# g12: g11 + P7 epilogue without the 32 zero-inits of packed fp8 words; 8 instead of 32 s_nop states before the fp8 epilogues
# baseline (speedup 1.0000x reference)
.LBB0_614:
	s_nop 7
	v_add_u32_e32 v2, s65, v185
	ds_read_b128 v[14:17], v2
	ds_read_b128 v[10:13], v2 offset:16
	ds_read_b128 v[6:9], v2 offset:32
	ds_read_b128 v[2:5], v2 offset:48
	v_lshl_add_u32 v20, s64, 8, v184
	s_waitcnt lgkmcnt(0)
	v_mov_b32_e32 v226, 1.0
	v_mov_b32_e32 v227, 1.0
	v_pk_add_f32 v[158:159], v[158:159], v[14:15]
	v_pk_add_f32 v[160:161], v[160:161], v[16:17]
	v_pk_add_f32 v[154:155], v[154:155], v[10:11]
	v_pk_add_f32 v[156:157], v[156:157], v[12:13]
	v_pk_add_f32 v[150:151], v[150:151], v[6:7]
	v_pk_add_f32 v[152:153], v[152:153], v[8:9]
	v_pk_add_f32 v[146:147], v[146:147], v[2:3]
	v_pk_add_f32 v[148:149], v[148:149], v[4:5]
	v_min_f32_e32 v158, 0x40e00000, v158
	v_min_f32_e32 v160, 0x40e00000, v160
	v_min_f32_e32 v154, 0x40e00000, v154
	v_min_f32_e32 v156, 0x40e00000, v156
	v_min_f32_e32 v150, 0x40e00000, v150
	v_min_f32_e32 v152, 0x40e00000, v152
	v_min_f32_e32 v146, 0x40e00000, v146
	v_min_f32_e32 v148, 0x40e00000, v148
	v_mul_f32_e32 v206, 0xc01d265f, v158
	v_mul_f32_e32 v208, 0xc01d265f, v160
	v_mul_f32_e32 v210, 0xc01d265f, v154
	v_mul_f32_e32 v212, 0xc01d265f, v156
	v_mul_f32_e32 v214, 0xc01d265f, v150
	v_mul_f32_e32 v216, 0xc01d265f, v152
	v_mul_f32_e32 v218, 0xc01d265f, v146
	v_mul_f32_e32 v220, 0xc01d265f, v148
	v_exp_f32_e32 v206, v206
	v_exp_f32_e32 v208, v208
	v_exp_f32_e32 v210, v210
	v_exp_f32_e32 v212, v212
	v_exp_f32_e32 v214, v214
	v_exp_f32_e32 v216, v216
	v_exp_f32_e32 v218, v218
	v_exp_f32_e32 v220, v220
	v_med3_f32 v207, v159, s58, v195
	v_med3_f32 v209, v161, s58, v195
	v_med3_f32 v211, v155, s58, v195
	v_med3_f32 v213, v157, s58, v195
	v_med3_f32 v215, v151, s58, v195
	v_med3_f32 v217, v153, s58, v195
	v_med3_f32 v219, v147, s58, v195
	v_med3_f32 v221, v149, s58, v195
	v_pk_add_f32 v[206:207], v[206:207], v[226:227]
	v_pk_add_f32 v[208:209], v[208:209], v[226:227]
	v_pk_add_f32 v[210:211], v[210:211], v[226:227]
	v_pk_add_f32 v[212:213], v[212:213], v[226:227]
	v_pk_add_f32 v[214:215], v[214:215], v[226:227]
	v_pk_add_f32 v[216:217], v[216:217], v[226:227]
	v_pk_add_f32 v[218:219], v[218:219], v[226:227]
	v_pk_add_f32 v[220:221], v[220:221], v[226:227]
	v_rcp_f32_e32 v206, v206
	v_rcp_f32_e32 v208, v208
	v_rcp_f32_e32 v210, v210
	v_rcp_f32_e32 v212, v212
	v_rcp_f32_e32 v214, v214
	v_rcp_f32_e32 v216, v216
	v_rcp_f32_e32 v218, v218
	v_rcp_f32_e32 v220, v220
	v_mul_f32_e32 v158, v158, v206
	v_mul_f32_e32 v160, v160, v208
	v_mul_f32_e32 v154, v154, v210
	v_mul_f32_e32 v156, v156, v212
	v_mul_f32_e32 v150, v150, v214
	v_mul_f32_e32 v152, v152, v216
	v_mul_f32_e32 v146, v146, v218
	v_mul_f32_e32 v148, v148, v220
	v_mul_f32_e32 v158, v207, v158
	v_mul_f32_e32 v160, v209, v160
	v_mul_f32_e32 v154, v211, v154
	v_mul_f32_e32 v156, v213, v156
	v_mul_f32_e32 v150, v215, v150
	v_mul_f32_e32 v152, v217, v152
	v_mul_f32_e32 v146, v219, v146
	v_mul_f32_e32 v148, v221, v148
	v_cvt_pk_fp8_f32 v222, v158, v160
	v_cvt_pk_fp8_f32 v223, v150, v152
	s_lshl_b32 s4, s38, 7
	v_ashrrev_i32_e32 v21, 31, v20
	s_and_b32 s4, s4, 0x780
	v_lshlrev_b64 v[18:19], 11, v[20:21]
	v_or_b32_e32 v168, s4, v183
	v_lshl_add_u64 v[18:19], s[14:15], 0, v[18:19]
	v_lshl_add_u64 v[18:19], v[18:19], 0, v[168:169]
	v_cvt_pk_fp8_f32 v222, v154, v156 op_sel:[0,0,1]
	v_cvt_pk_fp8_f32 v223, v146, v148 op_sel:[0,0,1]
	global_store_dwordx2 v[18:19], v[222:223], off
	v_pk_add_f32 v[142:143], v[142:143], v[14:15]
	v_pk_add_f32 v[144:145], v[144:145], v[16:17]
	v_pk_add_f32 v[138:139], v[138:139], v[10:11]
	v_pk_add_f32 v[140:141], v[140:141], v[12:13]
	v_pk_add_f32 v[134:135], v[134:135], v[6:7]
	v_pk_add_f32 v[136:137], v[136:137], v[8:9]
	v_pk_add_f32 v[130:131], v[130:131], v[2:3]
	v_pk_add_f32 v[132:133], v[132:133], v[4:5]
	v_min_f32_e32 v142, 0x40e00000, v142
	v_min_f32_e32 v144, 0x40e00000, v144
	v_min_f32_e32 v138, 0x40e00000, v138
	v_min_f32_e32 v140, 0x40e00000, v140
	v_min_f32_e32 v134, 0x40e00000, v134
	v_min_f32_e32 v136, 0x40e00000, v136
	v_min_f32_e32 v130, 0x40e00000, v130
	v_min_f32_e32 v132, 0x40e00000, v132
	v_mul_f32_e32 v206, 0xc01d265f, v142
	v_mul_f32_e32 v208, 0xc01d265f, v144
	v_mul_f32_e32 v210, 0xc01d265f, v138
	v_mul_f32_e32 v212, 0xc01d265f, v140
	v_mul_f32_e32 v214, 0xc01d265f, v134
	v_mul_f32_e32 v216, 0xc01d265f, v136
	v_mul_f32_e32 v218, 0xc01d265f, v130
	v_mul_f32_e32 v220, 0xc01d265f, v132
	v_exp_f32_e32 v206, v206
	v_exp_f32_e32 v208, v208
	v_exp_f32_e32 v210, v210
	v_exp_f32_e32 v212, v212
	v_exp_f32_e32 v214, v214
	v_exp_f32_e32 v216, v216
	v_exp_f32_e32 v218, v218
	v_exp_f32_e32 v220, v220
	v_med3_f32 v207, v143, s58, v195
	v_med3_f32 v209, v145, s58, v195
	v_med3_f32 v211, v139, s58, v195
	v_med3_f32 v213, v141, s58, v195
	v_med3_f32 v215, v135, s58, v195
	v_med3_f32 v217, v137, s58, v195
	v_med3_f32 v219, v131, s58, v195
	v_med3_f32 v221, v133, s58, v195
	v_pk_add_f32 v[206:207], v[206:207], v[226:227]
	v_pk_add_f32 v[208:209], v[208:209], v[226:227]
	v_pk_add_f32 v[210:211], v[210:211], v[226:227]
	v_pk_add_f32 v[212:213], v[212:213], v[226:227]
	v_pk_add_f32 v[214:215], v[214:215], v[226:227]
	v_pk_add_f32 v[216:217], v[216:217], v[226:227]
	v_pk_add_f32 v[218:219], v[218:219], v[226:227]
	v_pk_add_f32 v[220:221], v[220:221], v[226:227]
	v_rcp_f32_e32 v206, v206
	v_rcp_f32_e32 v208, v208
	v_rcp_f32_e32 v210, v210
	v_rcp_f32_e32 v212, v212
	v_rcp_f32_e32 v214, v214
	v_rcp_f32_e32 v216, v216
	v_rcp_f32_e32 v218, v218
	v_rcp_f32_e32 v220, v220
	v_mul_f32_e32 v142, v142, v206
	v_mul_f32_e32 v144, v144, v208
	v_mul_f32_e32 v138, v138, v210
	v_mul_f32_e32 v140, v140, v212
	v_mul_f32_e32 v134, v134, v214
	v_mul_f32_e32 v136, v136, v216
	v_mul_f32_e32 v130, v130, v218
	v_mul_f32_e32 v132, v132, v220
	v_mul_f32_e32 v142, v207, v142
	v_mul_f32_e32 v144, v209, v144
	v_mul_f32_e32 v138, v211, v138
	v_mul_f32_e32 v140, v213, v140
	v_mul_f32_e32 v134, v215, v134
	v_mul_f32_e32 v136, v217, v136
	v_mul_f32_e32 v130, v219, v130
	v_mul_f32_e32 v132, v221, v132
	v_cvt_pk_fp8_f32 v222, v142, v144
	v_cvt_pk_fp8_f32 v223, v134, v136
	v_or_b32_e32 v224, 16, v20
	v_ashrrev_i32_e32 v225, 31, v224
	v_lshlrev_b64 v[224:225], 11, v[224:225]
	v_lshl_add_u64 v[224:225], s[14:15], 0, v[224:225]
	v_lshl_add_u64 v[224:225], v[224:225], 0, v[168:169]
	v_cvt_pk_fp8_f32 v222, v138, v140 op_sel:[0,0,1]
	v_cvt_pk_fp8_f32 v223, v130, v132 op_sel:[0,0,1]
	global_store_dwordx2 v[224:225], v[222:223], off
	v_pk_add_f32 v[126:127], v[126:127], v[14:15]
	v_pk_add_f32 v[128:129], v[128:129], v[16:17]
	v_pk_add_f32 v[122:123], v[122:123], v[10:11]
	v_pk_add_f32 v[124:125], v[124:125], v[12:13]
	v_pk_add_f32 v[118:119], v[118:119], v[6:7]
	v_pk_add_f32 v[120:121], v[120:121], v[8:9]
	v_pk_add_f32 v[114:115], v[114:115], v[2:3]
	v_pk_add_f32 v[116:117], v[116:117], v[4:5]
	v_min_f32_e32 v126, 0x40e00000, v126
	v_min_f32_e32 v128, 0x40e00000, v128
	v_min_f32_e32 v122, 0x40e00000, v122
	v_min_f32_e32 v124, 0x40e00000, v124
	v_min_f32_e32 v118, 0x40e00000, v118
	v_min_f32_e32 v120, 0x40e00000, v120
	v_min_f32_e32 v114, 0x40e00000, v114
	v_min_f32_e32 v116, 0x40e00000, v116
	v_mul_f32_e32 v206, 0xc01d265f, v126
	v_mul_f32_e32 v208, 0xc01d265f, v128
	v_mul_f32_e32 v210, 0xc01d265f, v122
	v_mul_f32_e32 v212, 0xc01d265f, v124
	v_mul_f32_e32 v214, 0xc01d265f, v118
	v_mul_f32_e32 v216, 0xc01d265f, v120
	v_mul_f32_e32 v218, 0xc01d265f, v114
	v_mul_f32_e32 v220, 0xc01d265f, v116
	v_exp_f32_e32 v206, v206
	v_exp_f32_e32 v208, v208
	v_exp_f32_e32 v210, v210
	v_exp_f32_e32 v212, v212
	v_exp_f32_e32 v214, v214
	v_exp_f32_e32 v216, v216
	v_exp_f32_e32 v218, v218
	v_exp_f32_e32 v220, v220
	v_med3_f32 v207, v127, s58, v195
	v_med3_f32 v209, v129, s58, v195
	v_med3_f32 v211, v123, s58, v195
	v_med3_f32 v213, v125, s58, v195
	v_med3_f32 v215, v119, s58, v195
	v_med3_f32 v217, v121, s58, v195
	v_med3_f32 v219, v115, s58, v195
	v_med3_f32 v221, v117, s58, v195
	v_pk_add_f32 v[206:207], v[206:207], v[226:227]
	v_pk_add_f32 v[208:209], v[208:209], v[226:227]
	v_pk_add_f32 v[210:211], v[210:211], v[226:227]
	v_pk_add_f32 v[212:213], v[212:213], v[226:227]
	v_pk_add_f32 v[214:215], v[214:215], v[226:227]
	v_pk_add_f32 v[216:217], v[216:217], v[226:227]
	v_pk_add_f32 v[218:219], v[218:219], v[226:227]
	v_pk_add_f32 v[220:221], v[220:221], v[226:227]
	v_rcp_f32_e32 v206, v206
	v_rcp_f32_e32 v208, v208
	v_rcp_f32_e32 v210, v210
	v_rcp_f32_e32 v212, v212
	v_rcp_f32_e32 v214, v214
	v_rcp_f32_e32 v216, v216
	v_rcp_f32_e32 v218, v218
	v_rcp_f32_e32 v220, v220
	v_mul_f32_e32 v126, v126, v206
	v_mul_f32_e32 v128, v128, v208
	v_mul_f32_e32 v122, v122, v210
	v_mul_f32_e32 v124, v124, v212
	v_mul_f32_e32 v118, v118, v214
	v_mul_f32_e32 v120, v120, v216
	v_mul_f32_e32 v114, v114, v218
	v_mul_f32_e32 v116, v116, v220
	v_mul_f32_e32 v126, v207, v126
	v_mul_f32_e32 v128, v209, v128
	v_mul_f32_e32 v122, v211, v122
	v_mul_f32_e32 v124, v213, v124
	v_mul_f32_e32 v118, v215, v118
	v_mul_f32_e32 v120, v217, v120
	v_mul_f32_e32 v114, v219, v114
	v_mul_f32_e32 v116, v221, v116
	v_cvt_pk_fp8_f32 v222, v126, v128
	v_cvt_pk_fp8_f32 v223, v118, v120
	v_or_b32_e32 v224, 32, v20
	v_ashrrev_i32_e32 v225, 31, v224
	v_lshlrev_b64 v[224:225], 11, v[224:225]
	v_lshl_add_u64 v[224:225], s[14:15], 0, v[224:225]
	v_lshl_add_u64 v[224:225], v[224:225], 0, v[168:169]
	v_cvt_pk_fp8_f32 v222, v122, v124 op_sel:[0,0,1]
	v_cvt_pk_fp8_f32 v223, v114, v116 op_sel:[0,0,1]
	global_store_dwordx2 v[224:225], v[222:223], off
	v_pk_add_f32 v[110:111], v[110:111], v[14:15]
	v_pk_add_f32 v[112:113], v[112:113], v[16:17]
	v_pk_add_f32 v[106:107], v[106:107], v[10:11]
	v_pk_add_f32 v[108:109], v[108:109], v[12:13]
	v_pk_add_f32 v[98:99], v[98:99], v[6:7]
	v_pk_add_f32 v[100:101], v[100:101], v[8:9]
	v_pk_add_f32 v[90:91], v[90:91], v[2:3]
	v_pk_add_f32 v[92:93], v[92:93], v[4:5]
	v_min_f32_e32 v110, 0x40e00000, v110
	v_min_f32_e32 v112, 0x40e00000, v112
	v_min_f32_e32 v106, 0x40e00000, v106
	v_min_f32_e32 v108, 0x40e00000, v108
	v_min_f32_e32 v98, 0x40e00000, v98
	v_min_f32_e32 v100, 0x40e00000, v100
	v_min_f32_e32 v90, 0x40e00000, v90
	v_min_f32_e32 v92, 0x40e00000, v92
	v_mul_f32_e32 v206, 0xc01d265f, v110
	v_mul_f32_e32 v208, 0xc01d265f, v112
	v_mul_f32_e32 v210, 0xc01d265f, v106
	v_mul_f32_e32 v212, 0xc01d265f, v108
	v_mul_f32_e32 v214, 0xc01d265f, v98
	v_mul_f32_e32 v216, 0xc01d265f, v100
	v_mul_f32_e32 v218, 0xc01d265f, v90
	v_mul_f32_e32 v220, 0xc01d265f, v92
	v_exp_f32_e32 v206, v206
	v_exp_f32_e32 v208, v208
	v_exp_f32_e32 v210, v210
	v_exp_f32_e32 v212, v212
	v_exp_f32_e32 v214, v214
	v_exp_f32_e32 v216, v216
	v_exp_f32_e32 v218, v218
	v_exp_f32_e32 v220, v220
	v_med3_f32 v207, v111, s58, v195
	v_med3_f32 v209, v113, s58, v195
	v_med3_f32 v211, v107, s58, v195
	v_med3_f32 v213, v109, s58, v195
	v_med3_f32 v215, v99, s58, v195
	v_med3_f32 v217, v101, s58, v195
	v_med3_f32 v219, v91, s58, v195
	v_med3_f32 v221, v93, s58, v195
	v_pk_add_f32 v[206:207], v[206:207], v[226:227]
	v_pk_add_f32 v[208:209], v[208:209], v[226:227]
	v_pk_add_f32 v[210:211], v[210:211], v[226:227]
	v_pk_add_f32 v[212:213], v[212:213], v[226:227]
	v_pk_add_f32 v[214:215], v[214:215], v[226:227]
	v_pk_add_f32 v[216:217], v[216:217], v[226:227]
	v_pk_add_f32 v[218:219], v[218:219], v[226:227]
	v_pk_add_f32 v[220:221], v[220:221], v[226:227]
	v_rcp_f32_e32 v206, v206
	v_rcp_f32_e32 v208, v208
	v_rcp_f32_e32 v210, v210
	v_rcp_f32_e32 v212, v212
	v_rcp_f32_e32 v214, v214
	v_rcp_f32_e32 v216, v216
	v_rcp_f32_e32 v218, v218
	v_rcp_f32_e32 v220, v220
	v_mul_f32_e32 v110, v110, v206
	v_mul_f32_e32 v112, v112, v208
	v_mul_f32_e32 v106, v106, v210
	v_mul_f32_e32 v108, v108, v212
	v_mul_f32_e32 v98, v98, v214
	v_mul_f32_e32 v100, v100, v216
	v_mul_f32_e32 v90, v90, v218
	v_mul_f32_e32 v92, v92, v220
	v_mul_f32_e32 v110, v207, v110
	v_mul_f32_e32 v112, v209, v112
	v_mul_f32_e32 v106, v211, v106
	v_mul_f32_e32 v108, v213, v108
	v_mul_f32_e32 v98, v215, v98
	v_mul_f32_e32 v100, v217, v100
	v_mul_f32_e32 v90, v219, v90
	v_mul_f32_e32 v92, v221, v92
	v_cvt_pk_fp8_f32 v222, v110, v112
	v_cvt_pk_fp8_f32 v223, v98, v100
	v_or_b32_e32 v224, 48, v20
	v_ashrrev_i32_e32 v225, 31, v224
	v_lshlrev_b64 v[224:225], 11, v[224:225]
	v_lshl_add_u64 v[224:225], s[14:15], 0, v[224:225]
	v_lshl_add_u64 v[224:225], v[224:225], 0, v[168:169]
	v_cvt_pk_fp8_f32 v222, v106, v108 op_sel:[0,0,1]
	v_cvt_pk_fp8_f32 v223, v90, v92 op_sel:[0,0,1]
	global_store_dwordx2 v[224:225], v[222:223], off
	v_pk_add_f32 v[102:103], v[102:103], v[14:15]
	v_pk_add_f32 v[104:105], v[104:105], v[16:17]
	v_pk_add_f32 v[94:95], v[94:95], v[10:11]
	v_pk_add_f32 v[96:97], v[96:97], v[12:13]
	v_pk_add_f32 v[86:87], v[86:87], v[6:7]
	v_pk_add_f32 v[88:89], v[88:89], v[8:9]
	v_pk_add_f32 v[82:83], v[82:83], v[2:3]
	v_pk_add_f32 v[84:85], v[84:85], v[4:5]
	v_min_f32_e32 v102, 0x40e00000, v102
	v_min_f32_e32 v104, 0x40e00000, v104
	v_min_f32_e32 v94, 0x40e00000, v94
	v_min_f32_e32 v96, 0x40e00000, v96
	v_min_f32_e32 v86, 0x40e00000, v86
	v_min_f32_e32 v88, 0x40e00000, v88
	v_min_f32_e32 v82, 0x40e00000, v82
	v_min_f32_e32 v84, 0x40e00000, v84
	v_mul_f32_e32 v206, 0xc01d265f, v102
	v_mul_f32_e32 v208, 0xc01d265f, v104
	v_mul_f32_e32 v210, 0xc01d265f, v94
	v_mul_f32_e32 v212, 0xc01d265f, v96
	v_mul_f32_e32 v214, 0xc01d265f, v86
	v_mul_f32_e32 v216, 0xc01d265f, v88
	v_mul_f32_e32 v218, 0xc01d265f, v82
	v_mul_f32_e32 v220, 0xc01d265f, v84
	v_exp_f32_e32 v206, v206
	v_exp_f32_e32 v208, v208
	v_exp_f32_e32 v210, v210
	v_exp_f32_e32 v212, v212
	v_exp_f32_e32 v214, v214
	v_exp_f32_e32 v216, v216
	v_exp_f32_e32 v218, v218
	v_exp_f32_e32 v220, v220
	v_med3_f32 v207, v103, s58, v195
	v_med3_f32 v209, v105, s58, v195
	v_med3_f32 v211, v95, s58, v195
	v_med3_f32 v213, v97, s58, v195
	v_med3_f32 v215, v87, s58, v195
	v_med3_f32 v217, v89, s58, v195
	v_med3_f32 v219, v83, s58, v195
	v_med3_f32 v221, v85, s58, v195
	v_pk_add_f32 v[206:207], v[206:207], v[226:227]
	v_pk_add_f32 v[208:209], v[208:209], v[226:227]
	v_pk_add_f32 v[210:211], v[210:211], v[226:227]
	v_pk_add_f32 v[212:213], v[212:213], v[226:227]
	v_pk_add_f32 v[214:215], v[214:215], v[226:227]
	v_pk_add_f32 v[216:217], v[216:217], v[226:227]
	v_pk_add_f32 v[218:219], v[218:219], v[226:227]
	v_pk_add_f32 v[220:221], v[220:221], v[226:227]
	v_rcp_f32_e32 v206, v206
	v_rcp_f32_e32 v208, v208
	v_rcp_f32_e32 v210, v210
	v_rcp_f32_e32 v212, v212
	v_rcp_f32_e32 v214, v214
	v_rcp_f32_e32 v216, v216
	v_rcp_f32_e32 v218, v218
	v_rcp_f32_e32 v220, v220
	v_mul_f32_e32 v102, v102, v206
	v_mul_f32_e32 v104, v104, v208
	v_mul_f32_e32 v94, v94, v210
	v_mul_f32_e32 v96, v96, v212
	v_mul_f32_e32 v86, v86, v214
	v_mul_f32_e32 v88, v88, v216
	v_mul_f32_e32 v82, v82, v218
	v_mul_f32_e32 v84, v84, v220
	v_mul_f32_e32 v102, v207, v102
	v_mul_f32_e32 v104, v209, v104
	v_mul_f32_e32 v94, v211, v94
	v_mul_f32_e32 v96, v213, v96
	v_mul_f32_e32 v86, v215, v86
	v_mul_f32_e32 v88, v217, v88
	v_mul_f32_e32 v82, v219, v82
	v_mul_f32_e32 v84, v221, v84
	v_cvt_pk_fp8_f32 v222, v102, v104
	v_cvt_pk_fp8_f32 v223, v86, v88
	v_add_co_u32_e32 v224, vcc, s59, v18
	s_nop 1
	v_addc_co_u32_e32 v225, vcc, 0, v19, vcc
	v_cvt_pk_fp8_f32 v222, v94, v96 op_sel:[0,0,1]
	v_cvt_pk_fp8_f32 v223, v82, v84 op_sel:[0,0,1]
	global_store_dwordx2 v[224:225], v[222:223], off
	v_pk_add_f32 v[78:79], v[78:79], v[14:15]
	v_pk_add_f32 v[80:81], v[80:81], v[16:17]
	v_pk_add_f32 v[74:75], v[74:75], v[10:11]
	v_pk_add_f32 v[76:77], v[76:77], v[12:13]
	v_pk_add_f32 v[70:71], v[70:71], v[6:7]
	v_pk_add_f32 v[72:73], v[72:73], v[8:9]
	v_pk_add_f32 v[66:67], v[66:67], v[2:3]
	v_pk_add_f32 v[68:69], v[68:69], v[4:5]
	v_min_f32_e32 v78, 0x40e00000, v78
	v_min_f32_e32 v80, 0x40e00000, v80
	v_min_f32_e32 v74, 0x40e00000, v74
	v_min_f32_e32 v76, 0x40e00000, v76
	v_min_f32_e32 v70, 0x40e00000, v70
	v_min_f32_e32 v72, 0x40e00000, v72
	v_min_f32_e32 v66, 0x40e00000, v66
	v_min_f32_e32 v68, 0x40e00000, v68
	v_mul_f32_e32 v206, 0xc01d265f, v78
	v_mul_f32_e32 v208, 0xc01d265f, v80
	v_mul_f32_e32 v210, 0xc01d265f, v74
	v_mul_f32_e32 v212, 0xc01d265f, v76
	v_mul_f32_e32 v214, 0xc01d265f, v70
	v_mul_f32_e32 v216, 0xc01d265f, v72
	v_mul_f32_e32 v218, 0xc01d265f, v66
	v_mul_f32_e32 v220, 0xc01d265f, v68
	v_exp_f32_e32 v206, v206
	v_exp_f32_e32 v208, v208
	v_exp_f32_e32 v210, v210
	v_exp_f32_e32 v212, v212
	v_exp_f32_e32 v214, v214
	v_exp_f32_e32 v216, v216
	v_exp_f32_e32 v218, v218
	v_exp_f32_e32 v220, v220
	v_med3_f32 v207, v79, s58, v195
	v_med3_f32 v209, v81, s58, v195
	v_med3_f32 v211, v75, s58, v195
	v_med3_f32 v213, v77, s58, v195
	v_med3_f32 v215, v71, s58, v195
	v_med3_f32 v217, v73, s58, v195
	v_med3_f32 v219, v67, s58, v195
	v_med3_f32 v221, v69, s58, v195
	v_pk_add_f32 v[206:207], v[206:207], v[226:227]
	v_pk_add_f32 v[208:209], v[208:209], v[226:227]
	v_pk_add_f32 v[210:211], v[210:211], v[226:227]
	v_pk_add_f32 v[212:213], v[212:213], v[226:227]
	v_pk_add_f32 v[214:215], v[214:215], v[226:227]
	v_pk_add_f32 v[216:217], v[216:217], v[226:227]
	v_pk_add_f32 v[218:219], v[218:219], v[226:227]
	v_pk_add_f32 v[220:221], v[220:221], v[226:227]
	v_rcp_f32_e32 v206, v206
	v_rcp_f32_e32 v208, v208
	v_rcp_f32_e32 v210, v210
	v_rcp_f32_e32 v212, v212
	v_rcp_f32_e32 v214, v214
	v_rcp_f32_e32 v216, v216
	v_rcp_f32_e32 v218, v218
	v_rcp_f32_e32 v220, v220
	v_mul_f32_e32 v78, v78, v206
	v_mul_f32_e32 v80, v80, v208
	v_mul_f32_e32 v74, v74, v210
	v_mul_f32_e32 v76, v76, v212
	v_mul_f32_e32 v70, v70, v214
	v_mul_f32_e32 v72, v72, v216
	v_mul_f32_e32 v66, v66, v218
	v_mul_f32_e32 v68, v68, v220
	v_mul_f32_e32 v78, v207, v78
	v_mul_f32_e32 v80, v209, v80
	v_mul_f32_e32 v74, v211, v74
	v_mul_f32_e32 v76, v213, v76
	v_mul_f32_e32 v70, v215, v70
	v_mul_f32_e32 v72, v217, v72
	v_mul_f32_e32 v66, v219, v66
	v_mul_f32_e32 v68, v221, v68
	v_cvt_pk_fp8_f32 v222, v78, v80
	v_cvt_pk_fp8_f32 v223, v70, v72
	v_add_co_u32_e32 v224, vcc, s60, v18
	s_nop 1
	v_addc_co_u32_e32 v225, vcc, 0, v19, vcc
	v_cvt_pk_fp8_f32 v222, v74, v76 op_sel:[0,0,1]
	v_cvt_pk_fp8_f32 v223, v66, v68 op_sel:[0,0,1]
	global_store_dwordx2 v[224:225], v[222:223], off
	v_pk_add_f32 v[62:63], v[62:63], v[14:15]
	v_pk_add_f32 v[64:65], v[64:65], v[16:17]
	v_pk_add_f32 v[58:59], v[58:59], v[10:11]
	v_pk_add_f32 v[60:61], v[60:61], v[12:13]
	v_pk_add_f32 v[54:55], v[54:55], v[6:7]
	v_pk_add_f32 v[56:57], v[56:57], v[8:9]
	v_pk_add_f32 v[50:51], v[50:51], v[2:3]
	v_pk_add_f32 v[52:53], v[52:53], v[4:5]
	v_min_f32_e32 v62, 0x40e00000, v62
	v_min_f32_e32 v64, 0x40e00000, v64
	v_min_f32_e32 v58, 0x40e00000, v58
	v_min_f32_e32 v60, 0x40e00000, v60
	v_min_f32_e32 v54, 0x40e00000, v54
	v_min_f32_e32 v56, 0x40e00000, v56
	v_min_f32_e32 v50, 0x40e00000, v50
	v_min_f32_e32 v52, 0x40e00000, v52
	v_mul_f32_e32 v206, 0xc01d265f, v62
	v_mul_f32_e32 v208, 0xc01d265f, v64
	v_mul_f32_e32 v210, 0xc01d265f, v58
	v_mul_f32_e32 v212, 0xc01d265f, v60
	v_mul_f32_e32 v214, 0xc01d265f, v54
	v_mul_f32_e32 v216, 0xc01d265f, v56
	v_mul_f32_e32 v218, 0xc01d265f, v50
	v_mul_f32_e32 v220, 0xc01d265f, v52
	v_exp_f32_e32 v206, v206
	v_exp_f32_e32 v208, v208
	v_exp_f32_e32 v210, v210
	v_exp_f32_e32 v212, v212
	v_exp_f32_e32 v214, v214
	v_exp_f32_e32 v216, v216
	v_exp_f32_e32 v218, v218
	v_exp_f32_e32 v220, v220
	v_med3_f32 v207, v63, s58, v195
	v_med3_f32 v209, v65, s58, v195
	v_med3_f32 v211, v59, s58, v195
	v_med3_f32 v213, v61, s58, v195
	v_med3_f32 v215, v55, s58, v195
	v_med3_f32 v217, v57, s58, v195
	v_med3_f32 v219, v51, s58, v195
	v_med3_f32 v221, v53, s58, v195
	v_pk_add_f32 v[206:207], v[206:207], v[226:227]
	v_pk_add_f32 v[208:209], v[208:209], v[226:227]
	v_pk_add_f32 v[210:211], v[210:211], v[226:227]
	v_pk_add_f32 v[212:213], v[212:213], v[226:227]
	v_pk_add_f32 v[214:215], v[214:215], v[226:227]
	v_pk_add_f32 v[216:217], v[216:217], v[226:227]
	v_pk_add_f32 v[218:219], v[218:219], v[226:227]
	v_pk_add_f32 v[220:221], v[220:221], v[226:227]
	v_rcp_f32_e32 v206, v206
	v_rcp_f32_e32 v208, v208
	v_rcp_f32_e32 v210, v210
	v_rcp_f32_e32 v212, v212
	v_rcp_f32_e32 v214, v214
	v_rcp_f32_e32 v216, v216
	v_rcp_f32_e32 v218, v218
	v_rcp_f32_e32 v220, v220
	v_mul_f32_e32 v62, v62, v206
	v_mul_f32_e32 v64, v64, v208
	v_mul_f32_e32 v58, v58, v210
	v_mul_f32_e32 v60, v60, v212
	v_mul_f32_e32 v54, v54, v214
	v_mul_f32_e32 v56, v56, v216
	v_mul_f32_e32 v50, v50, v218
	v_mul_f32_e32 v52, v52, v220
	v_mul_f32_e32 v62, v207, v62
	v_mul_f32_e32 v64, v209, v64
	v_mul_f32_e32 v58, v211, v58
	v_mul_f32_e32 v60, v213, v60
	v_mul_f32_e32 v54, v215, v54
	v_mul_f32_e32 v56, v217, v56
	v_mul_f32_e32 v50, v219, v50
	v_mul_f32_e32 v52, v221, v52
	v_cvt_pk_fp8_f32 v222, v62, v64
	v_cvt_pk_fp8_f32 v223, v54, v56
	v_add_co_u32_e32 v224, vcc, s61, v18
	s_nop 1
	v_addc_co_u32_e32 v225, vcc, 0, v19, vcc
	v_cvt_pk_fp8_f32 v222, v58, v60 op_sel:[0,0,1]
	v_cvt_pk_fp8_f32 v223, v50, v52 op_sel:[0,0,1]
	global_store_dwordx2 v[224:225], v[222:223], off
	v_pk_add_f32 v[46:47], v[46:47], v[14:15]
	v_pk_add_f32 v[48:49], v[48:49], v[16:17]
	v_pk_add_f32 v[42:43], v[42:43], v[10:11]
	v_pk_add_f32 v[44:45], v[44:45], v[12:13]
	v_pk_add_f32 v[38:39], v[38:39], v[6:7]
	v_pk_add_f32 v[40:41], v[40:41], v[8:9]
	v_pk_add_f32 v[34:35], v[34:35], v[2:3]
	v_pk_add_f32 v[36:37], v[36:37], v[4:5]
	v_min_f32_e32 v46, 0x40e00000, v46
	v_min_f32_e32 v48, 0x40e00000, v48
	v_min_f32_e32 v42, 0x40e00000, v42
	v_min_f32_e32 v44, 0x40e00000, v44
	v_min_f32_e32 v38, 0x40e00000, v38
	v_min_f32_e32 v40, 0x40e00000, v40
	v_min_f32_e32 v34, 0x40e00000, v34
	v_min_f32_e32 v36, 0x40e00000, v36
	v_mul_f32_e32 v206, 0xc01d265f, v46
	v_mul_f32_e32 v208, 0xc01d265f, v48
	v_mul_f32_e32 v210, 0xc01d265f, v42
	v_mul_f32_e32 v212, 0xc01d265f, v44
	v_mul_f32_e32 v214, 0xc01d265f, v38
	v_mul_f32_e32 v216, 0xc01d265f, v40
	v_mul_f32_e32 v218, 0xc01d265f, v34
	v_mul_f32_e32 v220, 0xc01d265f, v36
	v_exp_f32_e32 v206, v206
	v_exp_f32_e32 v208, v208
	v_exp_f32_e32 v210, v210
	v_exp_f32_e32 v212, v212
	v_exp_f32_e32 v214, v214
	v_exp_f32_e32 v216, v216
	v_exp_f32_e32 v218, v218
	v_exp_f32_e32 v220, v220
	v_med3_f32 v207, v47, s58, v195
	v_med3_f32 v209, v49, s58, v195
	v_med3_f32 v211, v43, s58, v195
	v_med3_f32 v213, v45, s58, v195
	v_med3_f32 v215, v39, s58, v195
	v_med3_f32 v217, v41, s58, v195
	v_med3_f32 v219, v35, s58, v195
	v_med3_f32 v221, v37, s58, v195
	v_pk_add_f32 v[206:207], v[206:207], v[226:227]
	v_pk_add_f32 v[208:209], v[208:209], v[226:227]
	v_pk_add_f32 v[210:211], v[210:211], v[226:227]
	v_pk_add_f32 v[212:213], v[212:213], v[226:227]
	v_pk_add_f32 v[214:215], v[214:215], v[226:227]
	v_pk_add_f32 v[216:217], v[216:217], v[226:227]
	v_pk_add_f32 v[218:219], v[218:219], v[226:227]
	v_pk_add_f32 v[220:221], v[220:221], v[226:227]
	v_rcp_f32_e32 v206, v206
	v_rcp_f32_e32 v208, v208
	v_rcp_f32_e32 v210, v210
	v_rcp_f32_e32 v212, v212
	v_rcp_f32_e32 v214, v214
	v_rcp_f32_e32 v216, v216
	v_rcp_f32_e32 v218, v218
	v_rcp_f32_e32 v220, v220
	v_mul_f32_e32 v46, v46, v206
	v_mul_f32_e32 v48, v48, v208
	v_mul_f32_e32 v42, v42, v210
	v_mul_f32_e32 v44, v44, v212
	v_mul_f32_e32 v38, v38, v214
	v_mul_f32_e32 v40, v40, v216
	v_mul_f32_e32 v34, v34, v218
	v_mul_f32_e32 v36, v36, v220
	v_mul_f32_e32 v46, v207, v46
	v_mul_f32_e32 v48, v209, v48
	v_mul_f32_e32 v42, v211, v42
	v_mul_f32_e32 v44, v213, v44
	v_mul_f32_e32 v38, v215, v38
	v_mul_f32_e32 v40, v217, v40
	v_mul_f32_e32 v34, v219, v34
	v_mul_f32_e32 v36, v221, v36
	v_cvt_pk_fp8_f32 v222, v46, v48
	v_cvt_pk_fp8_f32 v223, v38, v40
	v_add_co_u32_e32 v224, vcc, 0x58000, v18
	s_nop 1
	v_addc_co_u32_e32 v225, vcc, 0, v19, vcc
	v_cvt_pk_fp8_f32 v222, v42, v44 op_sel:[0,0,1]
	v_cvt_pk_fp8_f32 v223, v34, v36 op_sel:[0,0,1]
	global_store_dwordx2 v[224:225], v[222:223], off
	s_and_b64 vcc, exec, s[0:1]
	s_mov_b64 s[0:1], -1
	s_cbranch_vccnz .LBB0_603
	s_andn2_b64 vcc, exec, s[12:13]
	s_cbranch_vccnz .LBB0_602
	s_barrier
	s_branch .LBB0_602

.LBB0_712:
	s_add_i32 s4, s62, 0
	s_add_i32 s4, s4, 0x22400
	s_lshl_b32 s5, s54, 2
	s_add_i32 s5, s4, s5
	v_lshl_add_u32 v2, v1, 2, s5
	s_lshl_b32 s5, s53, 2
	s_add_i32 s4, s4, s5
	s_nop 7
	v_lshl_add_u32 v3, v187, 2, s4
	ds_read_b128 v[14:17], v2
	ds_read_b128 v[6:9], v2 offset:16
	v_add_u32_e32 v178, 0x400, v3
	ds_read2_b32 v[24:25], v178 offset1:16
	ds_read_b128 v[10:13], v2 offset:32
	ds_read_b128 v[2:5], v2 offset:48
	v_lshl_add_u32 v26, s30, 8, v190
	s_waitcnt lgkmcnt(0)
	v_pk_add_f32 v[20:21], v[160:161], v[16:17]
	v_mul_f32_e32 v18, 0x41800000, v24
	v_pk_mul_f32 v[28:29], v[20:21], v[18:19] op_sel_hi:[1,0]
	v_pk_add_f32 v[20:21], v[150:151], v[6:7]
	v_pk_add_f32 v[22:23], v[158:159], v[14:15]
	v_pk_mul_f32 v[30:31], v[20:21], v[18:19] op_sel_hi:[1,0]
	v_pk_mul_f32 v[22:23], v[22:23], v[18:19] op_sel_hi:[1,0]
	v_cvt_pk_fp8_f32 v21, v30, v31
	v_cvt_pk_fp8_f32 v20, v22, v23
	v_pk_add_f32 v[22:23], v[152:153], v[8:9]
	v_ashrrev_i32_e32 v27, 31, v26
	v_pk_mul_f32 v[22:23], v[22:23], v[18:19] op_sel_hi:[1,0]
	v_cvt_pk_fp8_f32 v20, v28, v29 op_sel:[0,0,1]
	v_cvt_pk_fp8_f32 v21, v22, v23 op_sel:[0,0,1]
	v_pk_add_f32 v[22:23], v[156:157], v[12:13]
	v_pk_add_f32 v[28:29], v[154:155], v[10:11]
	v_pk_mul_f32 v[30:31], v[22:23], v[18:19] op_sel_hi:[1,0]
	v_pk_add_f32 v[22:23], v[146:147], v[2:3]
	v_pk_mul_f32 v[28:29], v[28:29], v[18:19] op_sel_hi:[1,0]
	v_pk_mul_f32 v[32:33], v[22:23], v[18:19] op_sel_hi:[1,0]
	v_cvt_pk_fp8_f32 v22, v28, v29
	v_cvt_pk_fp8_f32 v23, v32, v33
	v_pk_add_f32 v[28:29], v[148:149], v[4:5]
	v_or_b32_e32 v172, s63, v191
	v_pk_mul_f32 v[18:19], v[28:29], v[18:19] op_sel_hi:[1,0]
	v_cvt_pk_fp8_f32 v22, v30, v31 op_sel:[0,0,1]
	v_cvt_pk_fp8_f32 v23, v18, v19 op_sel:[0,0,1]
	v_lshlrev_b64 v[18:19], 11, v[26:27]
	v_lshl_add_u64 v[18:19], s[12:13], 0, v[18:19]
	v_lshl_add_u64 v[18:19], v[18:19], 0, v[172:173]
	global_store_dwordx4 v[18:19], v[20:23], off
	v_mul_f32_e32 v24, 0x41800000, v25
	s_nop 0
	v_or_b32_e32 v20, 16, v26
	v_ashrrev_i32_e32 v21, 31, v20
	v_lshlrev_b64 v[28:29], 11, v[20:21]
	v_pk_add_f32 v[20:21], v[144:145], v[16:17]
	v_pk_add_f32 v[22:23], v[142:143], v[14:15]
	v_pk_mul_f32 v[30:31], v[20:21], v[24:25] op_sel_hi:[1,0]
	v_pk_add_f32 v[20:21], v[134:135], v[6:7]
	v_pk_mul_f32 v[22:23], v[22:23], v[24:25] op_sel_hi:[1,0]
	v_pk_mul_f32 v[32:33], v[20:21], v[24:25] op_sel_hi:[1,0]
	v_cvt_pk_fp8_f32 v21, v32, v33
	v_cvt_pk_fp8_f32 v20, v22, v23
	v_pk_add_f32 v[22:23], v[136:137], v[8:9]
	v_lshl_add_u64 v[28:29], s[12:13], 0, v[28:29]
	v_pk_mul_f32 v[22:23], v[22:23], v[24:25] op_sel_hi:[1,0]
	v_cvt_pk_fp8_f32 v20, v30, v31 op_sel:[0,0,1]
	v_cvt_pk_fp8_f32 v21, v22, v23 op_sel:[0,0,1]
	v_pk_add_f32 v[22:23], v[140:141], v[12:13]
	v_pk_add_f32 v[30:31], v[138:139], v[10:11]
	v_pk_mul_f32 v[32:33], v[22:23], v[24:25] op_sel_hi:[1,0]
	v_pk_add_f32 v[22:23], v[130:131], v[2:3]
	v_pk_mul_f32 v[30:31], v[30:31], v[24:25] op_sel_hi:[1,0]
	v_pk_mul_f32 v[130:131], v[22:23], v[24:25] op_sel_hi:[1,0]
	v_cvt_pk_fp8_f32 v23, v130, v131
	v_cvt_pk_fp8_f32 v22, v30, v31
	v_pk_add_f32 v[30:31], v[132:133], v[4:5]
	v_lshl_add_u64 v[28:29], v[28:29], 0, v[172:173]
	v_pk_mul_f32 v[24:25], v[30:31], v[24:25] op_sel_hi:[1,0]
	v_cvt_pk_fp8_f32 v22, v32, v33 op_sel:[0,0,1]
	v_cvt_pk_fp8_f32 v23, v24, v25 op_sel:[0,0,1]
	ds_read2_b32 v[24:25], v178 offset0:32 offset1:48
	global_store_dwordx4 v[28:29], v[20:23], off
	s_nop 1
	v_pk_add_f32 v[20:21], v[128:129], v[16:17]
	s_waitcnt lgkmcnt(0)
	v_mul_f32_e32 v24, 0x41800000, v24
	v_pk_mul_f32 v[30:31], v[20:21], v[24:25] op_sel_hi:[1,0]
	v_pk_add_f32 v[20:21], v[118:119], v[6:7]
	v_pk_add_f32 v[22:23], v[126:127], v[14:15]
	v_pk_mul_f32 v[32:33], v[20:21], v[24:25] op_sel_hi:[1,0]
	v_pk_mul_f32 v[22:23], v[22:23], v[24:25] op_sel_hi:[1,0]
	v_cvt_pk_fp8_f32 v21, v32, v33
	v_cvt_pk_fp8_f32 v20, v22, v23
	v_pk_add_f32 v[22:23], v[120:121], v[8:9]
	v_or_b32_e32 v28, 32, v26
	v_pk_mul_f32 v[22:23], v[22:23], v[24:25] op_sel_hi:[1,0]
	v_cvt_pk_fp8_f32 v20, v30, v31 op_sel:[0,0,1]
	v_cvt_pk_fp8_f32 v21, v22, v23 op_sel:[0,0,1]
	v_pk_add_f32 v[22:23], v[124:125], v[12:13]
	v_pk_add_f32 v[30:31], v[122:123], v[10:11]
	v_pk_mul_f32 v[32:33], v[22:23], v[24:25] op_sel_hi:[1,0]
	v_pk_add_f32 v[22:23], v[110:111], v[2:3]
	v_pk_mul_f32 v[30:31], v[30:31], v[24:25] op_sel_hi:[1,0]
	v_pk_mul_f32 v[110:111], v[22:23], v[24:25] op_sel_hi:[1,0]
	v_cvt_pk_fp8_f32 v22, v30, v31
	v_cvt_pk_fp8_f32 v23, v110, v111
	v_pk_add_f32 v[30:31], v[112:113], v[4:5]
	v_ashrrev_i32_e32 v29, 31, v28
	v_pk_mul_f32 v[30:31], v[30:31], v[24:25] op_sel_hi:[1,0]
	v_cvt_pk_fp8_f32 v22, v32, v33 op_sel:[0,0,1]
	v_cvt_pk_fp8_f32 v23, v30, v31 op_sel:[0,0,1]
	v_lshlrev_b64 v[28:29], 11, v[28:29]
	v_lshl_add_u64 v[28:29], s[12:13], 0, v[28:29]
	v_lshl_add_u64 v[28:29], v[28:29], 0, v[172:173]
	global_store_dwordx4 v[28:29], v[20:23], off
	v_or_b32_e32 v24, 48, v26
	v_mul_f32_e32 v26, 0x41800000, v25
	v_pk_add_f32 v[20:21], v[96:97], v[16:17]
	v_pk_add_f32 v[22:23], v[94:95], v[14:15]
	v_pk_mul_f32 v[28:29], v[20:21], v[26:27] op_sel_hi:[1,0]
	v_pk_add_f32 v[20:21], v[78:79], v[6:7]
	v_pk_mul_f32 v[22:23], v[22:23], v[26:27] op_sel_hi:[1,0]
	v_pk_mul_f32 v[30:31], v[20:21], v[26:27] op_sel_hi:[1,0]
	v_cvt_pk_fp8_f32 v21, v30, v31
	v_cvt_pk_fp8_f32 v20, v22, v23
	v_pk_add_f32 v[22:23], v[80:81], v[8:9]
	v_ashrrev_i32_e32 v25, 31, v24
	v_pk_mul_f32 v[22:23], v[22:23], v[26:27] op_sel_hi:[1,0]
	v_cvt_pk_fp8_f32 v20, v28, v29 op_sel:[0,0,1]
	v_cvt_pk_fp8_f32 v21, v22, v23 op_sel:[0,0,1]
	v_pk_add_f32 v[22:23], v[92:93], v[12:13]
	v_pk_add_f32 v[28:29], v[90:91], v[10:11]
	v_pk_mul_f32 v[30:31], v[22:23], v[26:27] op_sel_hi:[1,0]
	v_pk_add_f32 v[22:23], v[74:75], v[2:3]
	v_pk_mul_f32 v[28:29], v[28:29], v[26:27] op_sel_hi:[1,0]
	v_pk_mul_f32 v[32:33], v[22:23], v[26:27] op_sel_hi:[1,0]
	v_cvt_pk_fp8_f32 v23, v32, v33
	v_cvt_pk_fp8_f32 v22, v28, v29
	v_pk_add_f32 v[28:29], v[76:77], v[4:5]
	v_lshlrev_b64 v[24:25], 11, v[24:25]
	v_pk_mul_f32 v[26:27], v[28:29], v[26:27] op_sel_hi:[1,0]
	v_cvt_pk_fp8_f32 v22, v30, v31 op_sel:[0,0,1]
	v_cvt_pk_fp8_f32 v23, v26, v27 op_sel:[0,0,1]
	ds_read2_b32 v[26:27], v178 offset0:128 offset1:144
	v_lshl_add_u64 v[24:25], s[12:13], 0, v[24:25]
	v_lshl_add_u64 v[24:25], v[24:25], 0, v[172:173]
	global_store_dwordx4 v[24:25], v[20:23], off
	s_waitcnt lgkmcnt(0)
	v_mul_f32_e32 v24, 0x41800000, v26
	v_pk_add_f32 v[20:21], v[116:117], v[16:17]
	v_pk_add_f32 v[22:23], v[114:115], v[14:15]
	v_pk_mul_f32 v[28:29], v[20:21], v[24:25] op_sel_hi:[1,0]
	v_pk_add_f32 v[20:21], v[102:103], v[6:7]
	v_pk_mul_f32 v[22:23], v[22:23], v[24:25] op_sel_hi:[1,0]
	v_pk_mul_f32 v[30:31], v[20:21], v[24:25] op_sel_hi:[1,0]
	v_cvt_pk_fp8_f32 v21, v30, v31
	v_cvt_pk_fp8_f32 v20, v22, v23
	v_pk_add_f32 v[22:23], v[104:105], v[8:9]
	v_cvt_pk_fp8_f32 v20, v28, v29 op_sel:[0,0,1]
	v_pk_mul_f32 v[22:23], v[22:23], v[24:25] op_sel_hi:[1,0]
	v_pk_add_f32 v[28:29], v[106:107], v[10:11]
	v_cvt_pk_fp8_f32 v21, v22, v23 op_sel:[0,0,1]
	v_pk_add_f32 v[22:23], v[108:109], v[12:13]
	v_pk_mul_f32 v[28:29], v[28:29], v[24:25] op_sel_hi:[1,0]
	v_pk_mul_f32 v[30:31], v[22:23], v[24:25] op_sel_hi:[1,0]
	v_pk_add_f32 v[22:23], v[98:99], v[2:3]
	s_nop 0
	v_pk_mul_f32 v[32:33], v[22:23], v[24:25] op_sel_hi:[1,0]
	v_cvt_pk_fp8_f32 v22, v28, v29
	v_cvt_pk_fp8_f32 v23, v32, v33
	v_pk_add_f32 v[28:29], v[100:101], v[4:5]
	v_cvt_pk_fp8_f32 v22, v30, v31 op_sel:[0,0,1]
	v_pk_mul_f32 v[24:25], v[28:29], v[24:25] op_sel_hi:[1,0]
	s_nop 0
	v_cvt_pk_fp8_f32 v23, v24, v25 op_sel:[0,0,1]
	v_add_co_u32_e32 v24, vcc, s58, v18
	s_nop 1
	v_addc_co_u32_e32 v25, vcc, 0, v19, vcc
	global_store_dwordx4 v[24:25], v[20:23], off
	v_mul_f32_e32 v24, 0x41800000, v27
	s_nop 0
	v_pk_add_f32 v[20:21], v[88:89], v[16:17]
	v_pk_add_f32 v[22:23], v[86:87], v[14:15]
	v_pk_mul_f32 v[26:27], v[20:21], v[24:25] op_sel_hi:[1,0]
	v_pk_add_f32 v[20:21], v[70:71], v[6:7]
	v_pk_mul_f32 v[22:23], v[22:23], v[24:25] op_sel_hi:[1,0]
	v_pk_mul_f32 v[28:29], v[20:21], v[24:25] op_sel_hi:[1,0]
	v_cvt_pk_fp8_f32 v21, v28, v29
	v_cvt_pk_fp8_f32 v20, v22, v23
	v_pk_add_f32 v[22:23], v[72:73], v[8:9]
	v_cvt_pk_fp8_f32 v20, v26, v27 op_sel:[0,0,1]
	v_pk_mul_f32 v[22:23], v[22:23], v[24:25] op_sel_hi:[1,0]
	v_pk_add_f32 v[26:27], v[82:83], v[10:11]
	v_cvt_pk_fp8_f32 v21, v22, v23 op_sel:[0,0,1]
	v_pk_add_f32 v[22:23], v[84:85], v[12:13]
	v_pk_mul_f32 v[26:27], v[26:27], v[24:25] op_sel_hi:[1,0]
	v_pk_mul_f32 v[28:29], v[22:23], v[24:25] op_sel_hi:[1,0]
	v_pk_add_f32 v[22:23], v[66:67], v[2:3]
	s_nop 0
	v_pk_mul_f32 v[30:31], v[22:23], v[24:25] op_sel_hi:[1,0]
	v_cvt_pk_fp8_f32 v23, v30, v31
	v_cvt_pk_fp8_f32 v22, v26, v27
	v_pk_add_f32 v[26:27], v[68:69], v[4:5]
	v_cvt_pk_fp8_f32 v22, v28, v29 op_sel:[0,0,1]
	v_pk_mul_f32 v[24:25], v[26:27], v[24:25] op_sel_hi:[1,0]
	v_add_co_u32_e32 v26, vcc, s59, v18
	v_cvt_pk_fp8_f32 v23, v24, v25 op_sel:[0,0,1]
	ds_read2_b32 v[24:25], v178 offset0:160 offset1:176
	v_addc_co_u32_e32 v27, vcc, 0, v19, vcc
	global_store_dwordx4 v[26:27], v[20:23], off
	s_waitcnt lgkmcnt(0)
	v_mul_f32_e32 v24, 0x41800000, v24
	v_pk_add_f32 v[20:21], v[64:65], v[16:17]
	v_pk_add_f32 v[22:23], v[62:63], v[14:15]
	v_pk_mul_f32 v[26:27], v[20:21], v[24:25] op_sel_hi:[1,0]
	v_pk_add_f32 v[20:21], v[54:55], v[6:7]
	v_pk_mul_f32 v[22:23], v[22:23], v[24:25] op_sel_hi:[1,0]
	v_pk_mul_f32 v[28:29], v[20:21], v[24:25] op_sel_hi:[1,0]
	v_cvt_pk_fp8_f32 v21, v28, v29
	v_cvt_pk_fp8_f32 v20, v22, v23
	v_pk_add_f32 v[22:23], v[56:57], v[8:9]
	v_pk_add_f32 v[6:7], v[38:39], v[6:7]
	v_pk_mul_f32 v[22:23], v[22:23], v[24:25] op_sel_hi:[1,0]
	v_cvt_pk_fp8_f32 v20, v26, v27 op_sel:[0,0,1]
	v_cvt_pk_fp8_f32 v21, v22, v23 op_sel:[0,0,1]
	v_pk_add_f32 v[22:23], v[60:61], v[12:13]
	v_pk_add_f32 v[26:27], v[58:59], v[10:11]
	v_pk_mul_f32 v[28:29], v[22:23], v[24:25] op_sel_hi:[1,0]
	v_pk_add_f32 v[22:23], v[50:51], v[2:3]
	v_pk_mul_f32 v[26:27], v[26:27], v[24:25] op_sel_hi:[1,0]
	v_pk_mul_f32 v[30:31], v[22:23], v[24:25] op_sel_hi:[1,0]
	v_cvt_pk_fp8_f32 v22, v26, v27
	v_cvt_pk_fp8_f32 v23, v30, v31
	v_pk_add_f32 v[26:27], v[52:53], v[4:5]
	v_pk_add_f32 v[8:9], v[40:41], v[8:9]
	v_pk_mul_f32 v[26:27], v[26:27], v[24:25] op_sel_hi:[1,0]
	v_cvt_pk_fp8_f32 v22, v28, v29 op_sel:[0,0,1]
	v_cvt_pk_fp8_f32 v23, v26, v27 op_sel:[0,0,1]
	v_add_co_u32_e32 v26, vcc, s60, v18
	v_pk_add_f32 v[14:15], v[46:47], v[14:15]
	s_nop 0
	v_addc_co_u32_e32 v27, vcc, 0, v19, vcc
	global_store_dwordx4 v[26:27], v[20:23], off
	v_pk_add_f32 v[10:11], v[42:43], v[10:11]
	v_pk_add_f32 v[2:3], v[34:35], v[2:3]
	v_mul_f32_e32 v20, 0x41800000, v25
	v_pk_mul_f32 v[22:23], v[6:7], v[20:21] op_sel_hi:[1,0]
	v_cvt_pk_fp8_f32 v7, v22, v23
	v_pk_mul_f32 v[8:9], v[8:9], v[20:21] op_sel_hi:[1,0]
	v_pk_mul_f32 v[14:15], v[14:15], v[20:21] op_sel_hi:[1,0]
	v_cvt_pk_fp8_f32 v7, v8, v9 op_sel:[0,0,1]
	v_pk_add_f32 v[8:9], v[44:45], v[12:13]
	v_pk_mul_f32 v[10:11], v[10:11], v[20:21] op_sel_hi:[1,0]
	v_pk_mul_f32 v[12:13], v[8:9], v[20:21] op_sel_hi:[1,0]
	v_pk_mul_f32 v[2:3], v[2:3], v[20:21] op_sel_hi:[1,0]
	v_cvt_pk_fp8_f32 v6, v14, v15
	v_cvt_pk_fp8_f32 v8, v10, v11
	v_cvt_pk_fp8_f32 v9, v2, v3
	v_pk_add_f32 v[16:17], v[48:49], v[16:17]
	v_pk_add_f32 v[2:3], v[36:37], v[4:5]
	v_pk_mul_f32 v[16:17], v[16:17], v[20:21] op_sel_hi:[1,0]
	v_pk_mul_f32 v[2:3], v[2:3], v[20:21] op_sel_hi:[1,0]
	v_cvt_pk_fp8_f32 v6, v16, v17 op_sel:[0,0,1]
	v_cvt_pk_fp8_f32 v8, v12, v13 op_sel:[0,0,1]
	v_cvt_pk_fp8_f32 v9, v2, v3 op_sel:[0,0,1]
	v_add_co_u32_e32 v2, vcc, 0x58000, v18
	s_nop 1
	v_addc_co_u32_e32 v3, vcc, 0, v19, vcc
	s_andn2_b64 vcc, exec, s[0:1]
	s_mov_b64 s[0:1], -1
	global_store_dwordx4 v[2:3], v[6:9], off
	s_cbranch_vccnz .LBB0_699
	s_andn2_b64 vcc, exec, s[10:11]
	s_cbranch_vccnz .LBB0_698
	s_barrier
	s_branch .LBB0_698
